# H3: next pair's state prefetch issued after the pass's own input loads with a counted vmcnt(8) (the compiler's vmcnt(0) had serialised it)
# speedup vs baseline: 1.0574x; 1.0574x over previous
.LBB0_763:
	s_and_b32 s3, s9, 0xf0
	s_and_b32 s9, s10, 0x7fffff00
	s_bfe_u32 s2, s10, 0x40004
	s_or_b32 s3, s9, s3
	s_or_b32 s2, s3, s2
	s_lshl_b32 s2, s2, 1
	s_add_i32 s9, s2, s6
	s_ashr_i32 s2, s9, 9
	s_ashr_i32 s3, s2, 31
	s_lshl_b32 s10, s9, 6
	s_lshl_b64 s[2:3], s[2:3], 11
	s_and_b32 s10, s10, 0x7c0
	s_or_b32 s2, s2, s10
	v_mov_b32_e32 v37, s3
	v_or_b32_e32 v36, s2, v52
	s_lshl_b32 s2, s9, 2
	s_and_b32 s9, s2, 0x780
	v_lshlrev_b64 v[80:81], 12, v[36:37]
	v_lshl_or_b32 v80, s9, 1, v80
	v_lshl_add_u64 v[36:37], v[56:57], 0, v[80:81]
	global_load_dwordx4 v[48:51], v[36:37], off
	global_load_dwordx4 v[44:47], v[36:37], off offset:64
	global_load_dwordx4 v[40:43], v[36:37], off offset:128
	s_nop 0
	global_load_dwordx4 v[36:39], v[36:37], off offset:192
	v_lshl_add_u64 v[66:67], v[58:59], 0, v[80:81]
	v_lshl_add_u64 v[88:89], v[60:61], 0, v[80:81]
	global_load_dwordx2 v[100:101], v[66:67], off
	global_load_dwordx2 v[82:83], v[88:89], off
	global_load_dwordx2 v[106:107], v[66:67], off offset:32
	global_load_dwordx2 v[78:79], v[88:89], off offset:32
	global_load_dwordx2 v[98:99], v[66:67], off offset:64
	global_load_dwordx2 v[76:77], v[88:89], off offset:64
	global_load_dwordx2 v[96:97], v[66:67], off offset:96
	global_load_dwordx2 v[74:75], v[88:89], off offset:96
	global_load_dwordx2 v[104:105], v[66:67], off offset:128
	global_load_dwordx2 v[72:73], v[88:89], off offset:128
	global_load_dwordx2 v[108:109], v[66:67], off offset:160
	global_load_dwordx2 v[70:71], v[88:89], off offset:160
	global_load_dwordx2 v[112:113], v[66:67], off offset:192
	global_load_dwordx2 v[68:69], v[88:89], off offset:192
	global_load_dwordx2 v[116:117], v[66:67], off offset:224
	s_nop 0
	global_load_dwordx2 v[66:67], v[88:89], off offset:224
	ds_read_b128 v[88:91], v53
	ds_read_b128 v[92:95], v53 offset:64
	s_mov_b32 s2, 0xf800000
	s_lshl_b32 s34, s9, 2
	s_mov_b32 s9, s8
	s_mov_b32 s10, s7
	s_cmp_lg_u32 s100, 0
	s_cbranch_scc0 .Lh3_nonext
	global_load_dwordx4 v[4:7], v[28:29], off nt
	global_load_dwordx4 v[8:11], v[8:9], off nt
	global_load_dwordx4 v[12:15], v[12:13], off nt
	global_load_dwordx4 v[16:19], v[16:17], off nt
	global_load_dwordx4 v[20:23], v[20:21], off nt
	global_load_dwordx4 v[24:27], v[24:25], off nt
	global_load_dwordx4 v[28:31], v[30:31], off nt
	global_load_dwordx4 v[32:35], v[32:33], off nt
	s_waitcnt vmcnt(8)
	s_branch .Lh3_go

.Lh3_go:
	s_waitcnt lgkmcnt(0)
	v_mfma_f32_16x16x32_bf16 v[88:91], v[88:91], v[48:51], 0
	ds_read_b128 v[118:121], v53 offset:8768
	ds_read_b128 v[122:125], v53 offset:13120
	v_mfma_f32_16x16x32_bf16 v[88:91], v[92:95], v[44:47], v[88:91]
	ds_read_b128 v[92:95], v53 offset:128
	s_waitcnt lgkmcnt(0)
	v_mfma_f32_16x16x32_bf16 v[88:91], v[92:95], v[40:43], v[88:91]
	ds_read_b128 v[92:95], v53 offset:192
	s_waitcnt lgkmcnt(0)
	v_mfma_f32_16x16x32_bf16 v[88:91], v[92:95], v[36:39], v[88:91]
	v_lshlrev_b32_e32 v94, 16, v100
	v_and_b32_e32 v95, 0xffff0000, v100
	v_lshlrev_b32_e32 v92, 16, v101
	v_and_b32_e32 v93, 0xffff0000, v101
	s_nop 3
	v_pk_add_f32 v[92:93], v[90:91], v[92:93]
	v_pk_add_f32 v[94:95], v[88:89], v[94:95]
	ds_read_b128 v[88:91], v53 offset:4352
	ds_read_b128 v[100:103], v53 offset:4416
	s_waitcnt lgkmcnt(1)
	v_mfma_f32_16x16x32_bf16 v[88:91], v[88:91], v[48:51], 0
	s_waitcnt lgkmcnt(0)
	v_mfma_f32_16x16x32_bf16 v[88:91], v[100:103], v[44:47], v[88:91]
	ds_read_b128 v[100:103], v53 offset:4480
	s_waitcnt lgkmcnt(0)
	v_mfma_f32_16x16x32_bf16 v[88:91], v[100:103], v[40:43], v[88:91]
	ds_read_b128 v[100:103], v53 offset:4544
	s_waitcnt lgkmcnt(0)
	v_mfma_f32_16x16x32_bf16 v[100:103], v[100:103], v[36:39], v[88:91]
	s_nop 4
	v_lshlrev_b32_e32 v90, 16, v106
	v_and_b32_e32 v91, 0xffff0000, v106
	v_lshlrev_b32_e32 v88, 16, v107
	v_and_b32_e32 v89, 0xffff0000, v107
	v_pk_add_f32 v[90:91], v[100:101], v[90:91]
	v_pk_add_f32 v[88:89], v[102:103], v[88:89]
	v_mov_b32_e32 v102, v95
	v_mov_b32_e32 v103, v91
	v_mov_b32_e32 v100, v94
	v_mov_b32_e32 v101, v90
	v_pk_mul_f32 v[102:103], v[102:103], v[102:103]
	v_mov_b32_e32 v106, v93
	v_mov_b32_e32 v107, v89
	v_pk_fma_f32 v[100:101], v[100:101], v[100:101], v[102:103]
	v_mov_b32_e32 v102, v92
	v_mov_b32_e32 v103, v88
	v_pk_mul_f32 v[106:107], v[106:107], v[106:107]
	s_nop 0
	v_pk_fma_f32 v[102:103], v[102:103], v[102:103], v[106:107]
	s_nop 0
	v_pk_add_f32 v[110:111], v[100:101], v[102:103]
	ds_read_b128 v[100:103], v53 offset:8704
	s_waitcnt lgkmcnt(0)
	v_mfma_f32_16x16x32_bf16 v[100:103], v[100:103], v[48:51], 0
	v_pk_add_f32 v[110:111], v[110:111], v[110:111] op_sel:[0,1] op_sel_hi:[1,0]
	v_mfma_f32_16x16x32_bf16 v[100:103], v[118:121], v[44:47], v[100:103]
	ds_read_b128 v[118:121], v53 offset:8832
	s_waitcnt lgkmcnt(0)
	v_mfma_f32_16x16x32_bf16 v[100:103], v[118:121], v[40:43], v[100:103]
	ds_read_b128 v[118:121], v53 offset:8896
	s_waitcnt lgkmcnt(0)
	v_mfma_f32_16x16x32_bf16 v[118:121], v[118:121], v[36:39], v[100:103]
	s_nop 4
	v_lshlrev_b32_e32 v102, 16, v98
	v_and_b32_e32 v103, 0xffff0000, v98
	v_lshlrev_b32_e32 v98, 16, v99
	v_and_b32_e32 v99, 0xffff0000, v99
	v_pk_add_f32 v[100:101], v[120:121], v[98:99]
	v_pk_add_f32 v[102:103], v[118:119], v[102:103]
	ds_read_b128 v[118:121], v53 offset:13056
	s_waitcnt lgkmcnt(0)
	v_mfma_f32_16x16x32_bf16 v[118:121], v[118:121], v[48:51], 0
	v_mul_f32_e64 v98, v102, v102
	v_mul_f32_e64 v99, v103, v103
	v_pk_mul_f32 v[106:107], v[100:101], v[100:101]
	v_mfma_f32_16x16x32_bf16 v[118:121], v[122:125], v[44:47], v[118:121]
	ds_read_b128 v[122:125], v53 offset:13184
	v_pk_mov_b32 v[114:115], v[98:99], v[106:107] op_sel:[1,0]
	v_mov_b32_e32 v99, v107
	s_waitcnt lgkmcnt(0)
	v_mfma_f32_16x16x32_bf16 v[118:121], v[122:125], v[40:43], v[118:121]
	ds_read_b128 v[122:125], v53 offset:13248
	v_pk_add_f32 v[114:115], v[114:115], v[98:99]
	v_lshlrev_b32_e32 v98, 16, v96
	s_waitcnt lgkmcnt(0)
	v_mfma_f32_16x16x32_bf16 v[118:121], v[122:125], v[36:39], v[118:121]
	v_and_b32_e32 v99, 0xffff0000, v96
	v_lshlrev_b32_e32 v96, 16, v97
	v_and_b32_e32 v97, 0xffff0000, v97
	s_nop 4
	v_pk_add_f32 v[96:97], v[120:121], v[96:97]
	v_pk_add_f32 v[98:99], v[118:119], v[98:99]
	ds_read_b128 v[118:121], v53 offset:17408
	ds_read_b128 v[122:125], v53 offset:17472
	s_waitcnt lgkmcnt(1)
	v_mfma_f32_16x16x32_bf16 v[118:121], v[118:121], v[48:51], 0
	v_lshlrev_b32_e32 v106, 16, v104
	v_and_b32_e32 v107, 0xffff0000, v104
	v_lshlrev_b32_e32 v104, 16, v105
	s_waitcnt lgkmcnt(0)
	v_mfma_f32_16x16x32_bf16 v[118:121], v[122:125], v[44:47], v[118:121]
	ds_read_b128 v[122:125], v53 offset:17536
	v_and_b32_e32 v105, 0xffff0000, v105
	v_pk_add_f32 v[114:115], v[114:115], v[114:115] op_sel:[0,1] op_sel_hi:[1,0]
	s_waitcnt lgkmcnt(0)
	v_mfma_f32_16x16x32_bf16 v[118:121], v[122:125], v[40:43], v[118:121]
	ds_read_b128 v[122:125], v53 offset:17600
	s_waitcnt lgkmcnt(0)
	v_mfma_f32_16x16x32_bf16 v[118:121], v[122:125], v[36:39], v[118:121]
	ds_read_b128 v[124:127], v53 offset:21824
	s_nop 6
	v_pk_add_f32 v[106:107], v[118:119], v[106:107]
	s_nop 0
	v_mul_f32_e32 v2, v106, v106
	v_mul_f32_e32 v118, v107, v107
	v_pk_add_f32 v[104:105], v[120:121], v[104:105]
	v_mov_b32_e32 v111, v2
	v_mov_b32_e32 v115, v118
	v_mul_f32_e32 v2, v99, v99
	v_mul_f32_e32 v119, v104, v104
	v_pk_add_f32 v[110:111], v[110:111], v[114:115]
	v_pk_fma_f32 v[114:115], v[98:99], v[98:99], v[2:3] op_sel_hi:[1,1,0]
	v_mul_f32_e32 v2, v97, v97
	v_mul_f32_e32 v120, v105, v105
	v_mov_b32_e32 v115, v119
	v_pk_fma_f32 v[118:119], v[96:97], v[96:97], v[2:3] op_sel_hi:[1,1,0]
	s_nop 0
	v_mov_b32_e32 v119, v120
	ds_read_b128 v[120:123], v53 offset:21760
	s_waitcnt lgkmcnt(0)
	v_mfma_f32_16x16x32_bf16 v[120:123], v[120:123], v[48:51], 0
	v_add_f32_e64 v114, v114, v118
	v_add_f32_e64 v115, v115, v119
	v_pk_add_f32 v[118:119], v[110:111], v[114:115]
	v_mfma_f32_16x16x32_bf16 v[120:123], v[124:127], v[44:47], v[120:123]
	ds_read_b128 v[124:127], v53 offset:21888
	v_lshlrev_b32_e32 v110, 16, v108
	v_and_b32_e32 v111, 0xffff0000, v108
	s_waitcnt lgkmcnt(0)
	v_mfma_f32_16x16x32_bf16 v[120:123], v[124:127], v[40:43], v[120:123]
	ds_read_b128 v[124:127], v53 offset:21952
	v_lshlrev_b32_e32 v108, 16, v109
	v_and_b32_e32 v109, 0xffff0000, v109
	s_waitcnt lgkmcnt(0)
	v_mfma_f32_16x16x32_bf16 v[120:123], v[124:127], v[36:39], v[120:123]
	ds_read_b128 v[126:129], v53 offset:26176
	s_nop 6
	v_pk_add_f32 v[108:109], v[122:123], v[108:109]
	v_pk_add_f32 v[110:111], v[120:121], v[110:111]
	v_pk_mul_f32 v[120:121], v[108:109], v[108:109]
	v_pk_mul_f32 v[114:115], v[110:111], v[110:111]
	s_nop 0
	v_pk_mov_b32 v[122:123], v[114:115], v[120:121] op_sel:[1,0]
	v_mov_b32_e32 v115, v121
	v_pk_add_f32 v[120:121], v[122:123], v[114:115]
	ds_read_b128 v[122:125], v53 offset:26112
	s_waitcnt lgkmcnt(0)
	v_mfma_f32_16x16x32_bf16 v[122:125], v[122:125], v[48:51], 0
	v_lshlrev_b32_e32 v114, 16, v112
	v_and_b32_e32 v115, 0xffff0000, v112
	v_lshlrev_b32_e32 v112, 16, v113
	v_mfma_f32_16x16x32_bf16 v[122:125], v[126:129], v[44:47], v[122:125]
	ds_read_b128 v[126:129], v53 offset:26240
	v_and_b32_e32 v113, 0xffff0000, v113
	s_waitcnt lgkmcnt(0)
	v_mfma_f32_16x16x32_bf16 v[122:125], v[126:129], v[40:43], v[122:125]
	ds_read_b128 v[126:129], v53 offset:26304
	s_waitcnt lgkmcnt(0)
	v_mfma_f32_16x16x32_bf16 v[122:125], v[126:129], v[36:39], v[122:125]
	s_nop 7
	v_pk_add_f32 v[112:113], v[124:125], v[112:113]
	v_pk_add_f32 v[114:115], v[122:123], v[114:115]
	ds_read_b128 v[122:125], v53 offset:30464
	s_waitcnt lgkmcnt(0)
	v_mfma_f32_16x16x32_bf16 v[48:51], v[122:125], v[48:51], 0
	ds_read_b128 v[122:125], v53 offset:30528
	s_waitcnt lgkmcnt(0)
	v_mfma_f32_16x16x32_bf16 v[44:47], v[122:125], v[44:47], v[48:51]
	s_nop 4
	ds_read_b128 v[48:51], v53 offset:30592
	s_waitcnt lgkmcnt(0)
	v_mfma_f32_16x16x32_bf16 v[40:43], v[48:51], v[40:43], v[44:47]
	s_nop 2
	ds_read_b128 v[44:47], v53 offset:30656
	v_lshlrev_b32_e32 v50, 16, v83
	v_and_b32_e32 v51, 0xffff0000, v83
	s_waitcnt lgkmcnt(0)
	v_mfma_f32_16x16x32_bf16 v[38:41], v[44:47], v[36:39], v[40:43]
	s_nop 2
	v_lshlrev_b32_e32 v42, 16, v116
	v_and_b32_e32 v43, 0xffff0000, v116
	v_lshlrev_b32_e32 v36, 16, v117
	v_and_b32_e32 v37, 0xffff0000, v117
	s_nop 0
	v_pk_add_f32 v[38:39], v[38:39], v[42:43]
	v_pk_add_f32 v[36:37], v[40:41], v[36:37]
	v_mul_f32_e32 v2, v38, v38
	v_mul_f32_e32 v44, v39, v39
	v_pk_add_f32 v[40:41], v[118:119], v[118:119] op_sel:[0,1] op_sel_hi:[1,0]
	v_pk_add_f32 v[42:43], v[120:121], v[120:121] op_sel:[0,1] op_sel_hi:[1,0]
	v_mov_b32_e32 v41, v2
	v_mov_b32_e32 v43, v44
	v_mul_f32_e32 v2, v115, v115
	v_mul_f32_e32 v45, v36, v36
	v_pk_add_f32 v[40:41], v[40:41], v[42:43]
	v_pk_fma_f32 v[42:43], v[114:115], v[114:115], v[2:3] op_sel_hi:[1,1,0]
	v_mul_f32_e32 v2, v113, v113
	v_mul_f32_e32 v46, v37, v37
	v_mov_b32_e32 v43, v45
	v_pk_fma_f32 v[44:45], v[112:113], v[112:113], v[2:3] op_sel_hi:[1,1,0]
	v_and_b32_e32 v47, 0xffff0000, v82
	v_mov_b32_e32 v45, v46
	v_pk_add_f32 v[42:43], v[42:43], v[44:45]
	v_lshlrev_b32_e32 v46, 16, v82
	v_pk_add_f32 v[40:41], v[40:41], v[42:43]
	v_mul_f32_e32 v48, 0xbfb8aa3b, v46
	v_add_f32_e32 v2, v40, v41
	v_and_b32_e32 v41, 64, v229
	v_xor_b32_e32 v40, 16, v229
	v_add_u32_e32 v41, 64, v41
	v_cmp_lt_i32_e32 vcc, v40, v41
	v_mul_f32_e32 v49, 0xbfb8aa3b, v47
	v_mul_f32_e32 v82, 0xbfb8aa3b, v50
	v_cndmask_b32_e32 v40, v229, v40, vcc
	v_lshlrev_b32_e32 v40, 2, v40
	ds_bpermute_b32 v40, v40, v2
	v_mul_f32_e32 v83, 0xbfb8aa3b, v51
	v_exp_f32_e32 v48, v48
	v_exp_f32_e32 v49, v49
	v_exp_f32_e32 v82, v82
	s_waitcnt lgkmcnt(0)
	v_add_f32_e32 v2, v2, v40
	v_xor_b32_e32 v40, 32, v229
	v_cmp_lt_i32_e32 vcc, v40, v41
	v_exp_f32_e32 v83, v83
	v_add_f32_e32 v48, 1.0, v48
	v_cndmask_b32_e32 v40, v229, v40, vcc
	v_lshlrev_b32_e32 v40, 2, v40
	ds_bpermute_b32 v40, v40, v2
	v_add_f32_e32 v49, 1.0, v49
	v_add_f32_e32 v82, 1.0, v82
	v_add_f32_e32 v83, 1.0, v83
	v_rcp_f32_e32 v48, v48
	s_waitcnt lgkmcnt(0)
	v_add_f32_e32 v2, v2, v40
	v_fmamk_f32 v2, v2, 0x3c000000, v230
	v_cmp_gt_f32_e32 vcc, s2, v2
	v_mul_f32_e32 v40, 0x4f800000, v2
	v_rcp_f32_e32 v49, v49
	v_cndmask_b32_e32 v2, v2, v40, vcc
	v_sqrt_f32_e32 v40, v2
	v_rcp_f32_e32 v82, v82
	v_rcp_f32_e32 v83, v83
	v_pk_mul_f32 v[46:47], v[48:49], v[46:47]
	v_add_u32_e32 v41, -1, v40
	v_fma_f32 v42, -v41, v40, v2
	v_cmp_ge_f32_e64 s[2:3], 0, v42
	v_add_u32_e32 v42, 1, v40
	v_pk_mul_f32 v[48:49], v[82:83], v[50:51]
	v_cndmask_b32_e64 v41, v40, v41, s[2:3]
	v_fma_f32 v40, -v42, v40, v2
	v_cmp_lt_f32_e64 s[2:3], 0, v40
	s_nop 1
	v_cndmask_b32_e64 v40, v41, v42, s[2:3]
	v_mul_f32_e32 v41, 0x37800000, v40
	v_cndmask_b32_e32 v40, v40, v41, vcc
	v_cmp_class_f32_e32 vcc, v2, v231
	s_nop 1
	v_cndmask_b32_e32 v2, v40, v2, vcc
	v_div_scale_f32 v40, s[2:3], v2, v2, 1.0
	v_rcp_f32_e32 v41, v40
	s_nop 0
	v_fma_f32 v42, -v40, v41, 1.0
	v_fmac_f32_e32 v41, v42, v41
	v_div_scale_f32 v42, vcc, 1.0, v2, 1.0
	v_mul_f32_e32 v43, v42, v41
	v_fma_f32 v44, -v40, v43, v42
	v_fmac_f32_e32 v43, v44, v41
	v_fma_f32 v40, -v40, v43, v42
	v_div_fmas_f32 v40, v40, v41, v43
	v_div_fixup_f32 v2, v40, v2, 1.0
	v_lshl_add_u64 v[40:41], v[62:63], 0, s[34:35]
	global_load_dwordx4 v[42:45], v[40:41], off
	v_pk_mul_f32 v[50:51], v[92:93], v[2:3] op_sel_hi:[1,0]
	v_pk_mul_f32 v[82:83], v[94:95], v[2:3] op_sel_hi:[1,0]
	v_pk_mul_f32 v[36:37], v[36:37], v[2:3] op_sel_hi:[1,0]
	v_pk_mul_f32 v[38:39], v[38:39], v[2:3] op_sel_hi:[1,0]
	s_andn2_b64 vcc, exec, s[4:5]
	s_waitcnt vmcnt(0)
	v_pk_mul_f32 v[42:43], v[42:43], v[82:83]
	v_pk_mul_f32 v[44:45], v[44:45], v[50:51]
	v_pk_mul_f32 v[42:43], v[46:47], v[42:43]
	v_pk_mul_f32 v[44:45], v[48:49], v[44:45]
	v_cvt_pk_bf16_f32 v46, v42, v43
	v_cvt_pk_bf16_f32 v47, v44, v45
	v_lshl_add_u64 v[42:43], v[64:65], 0, v[80:81]
	global_store_dwordx2 v[42:43], v[46:47], off
	global_load_dwordx4 v[44:47], v[40:41], off offset:64
	v_lshlrev_b32_e32 v48, 16, v78
	v_and_b32_e32 v49, 0xffff0000, v78
	v_lshlrev_b32_e32 v78, 16, v79
	v_and_b32_e32 v79, 0xffff0000, v79
	v_mul_f32_e32 v50, 0xbfb8aa3b, v48
	v_mul_f32_e32 v51, 0xbfb8aa3b, v49
	v_mul_f32_e32 v80, 0xbfb8aa3b, v78
	v_mul_f32_e32 v81, 0xbfb8aa3b, v79
	v_exp_f32_e32 v50, v50
	v_exp_f32_e32 v51, v51
	v_exp_f32_e32 v80, v80
	v_exp_f32_e32 v81, v81
	v_add_f32_e32 v50, 1.0, v50
	v_add_f32_e32 v51, 1.0, v51
	v_add_f32_e32 v80, 1.0, v80
	v_add_f32_e32 v81, 1.0, v81
	v_rcp_f32_e32 v50, v50
	v_rcp_f32_e32 v51, v51
	v_rcp_f32_e32 v80, v80
	v_rcp_f32_e32 v81, v81
	v_pk_mul_f32 v[48:49], v[50:51], v[48:49]
	v_pk_mul_f32 v[50:51], v[80:81], v[78:79]
	v_pk_mul_f32 v[78:79], v[88:89], v[2:3] op_sel_hi:[1,0]
	v_pk_mul_f32 v[80:81], v[90:91], v[2:3] op_sel_hi:[1,0]
	s_waitcnt vmcnt(0)
	v_pk_mul_f32 v[46:47], v[46:47], v[78:79]
	v_pk_mul_f32 v[44:45], v[44:45], v[80:81]
	v_pk_mul_f32 v[46:47], v[50:51], v[46:47]
	v_pk_mul_f32 v[44:45], v[48:49], v[44:45]
	v_lshlrev_b32_e32 v48, 16, v76
	v_cvt_pk_bf16_f32 v44, v44, v45
	v_cvt_pk_bf16_f32 v45, v46, v47
	global_store_dwordx2 v[42:43], v[44:45], off offset:32
	global_load_dwordx4 v[44:47], v[40:41], off offset:128
	v_and_b32_e32 v49, 0xffff0000, v76
	v_lshlrev_b32_e32 v76, 16, v77
	v_and_b32_e32 v77, 0xffff0000, v77
	v_mul_f32_e32 v50, 0xbfb8aa3b, v48
	v_mul_f32_e32 v51, 0xbfb8aa3b, v49
	v_mul_f32_e32 v78, 0xbfb8aa3b, v76
	v_mul_f32_e32 v79, 0xbfb8aa3b, v77
	v_exp_f32_e32 v50, v50
	v_exp_f32_e32 v51, v51
	v_exp_f32_e32 v78, v78
	v_exp_f32_e32 v79, v79
	v_add_f32_e32 v50, 1.0, v50
	v_add_f32_e32 v51, 1.0, v51
	v_add_f32_e32 v78, 1.0, v78
	v_add_f32_e32 v79, 1.0, v79
	v_rcp_f32_e32 v50, v50
	v_rcp_f32_e32 v51, v51
	v_rcp_f32_e32 v78, v78
	v_rcp_f32_e32 v79, v79
	v_pk_mul_f32 v[48:49], v[50:51], v[48:49]
	v_pk_mul_f32 v[50:51], v[78:79], v[76:77]
	v_pk_mul_f32 v[76:77], v[100:101], v[2:3] op_sel_hi:[1,0]
	v_pk_mul_f32 v[78:79], v[102:103], v[2:3] op_sel_hi:[1,0]
	s_waitcnt vmcnt(0)
	v_pk_mul_f32 v[46:47], v[46:47], v[76:77]
	v_pk_mul_f32 v[44:45], v[44:45], v[78:79]
	v_pk_mul_f32 v[46:47], v[50:51], v[46:47]
	v_pk_mul_f32 v[44:45], v[48:49], v[44:45]
	v_lshlrev_b32_e32 v48, 16, v74
	v_cvt_pk_bf16_f32 v44, v44, v45
	v_cvt_pk_bf16_f32 v45, v46, v47
	global_store_dwordx2 v[42:43], v[44:45], off offset:64
	global_load_dwordx4 v[44:47], v[40:41], off offset:192
	v_and_b32_e32 v49, 0xffff0000, v74
	v_lshlrev_b32_e32 v74, 16, v75
	v_and_b32_e32 v75, 0xffff0000, v75
	v_mul_f32_e32 v50, 0xbfb8aa3b, v48
	v_mul_f32_e32 v51, 0xbfb8aa3b, v49
	v_mul_f32_e32 v76, 0xbfb8aa3b, v74
	v_mul_f32_e32 v77, 0xbfb8aa3b, v75
	v_exp_f32_e32 v50, v50
	v_exp_f32_e32 v51, v51
	v_exp_f32_e32 v76, v76
	v_exp_f32_e32 v77, v77
	v_add_f32_e32 v50, 1.0, v50
	v_add_f32_e32 v51, 1.0, v51
	v_add_f32_e32 v76, 1.0, v76
	v_add_f32_e32 v77, 1.0, v77
	v_rcp_f32_e32 v50, v50
	v_rcp_f32_e32 v51, v51
	v_rcp_f32_e32 v76, v76
	v_rcp_f32_e32 v77, v77
	v_pk_mul_f32 v[48:49], v[50:51], v[48:49]
	v_pk_mul_f32 v[50:51], v[76:77], v[74:75]
	v_pk_mul_f32 v[74:75], v[96:97], v[2:3] op_sel_hi:[1,0]
	v_pk_mul_f32 v[76:77], v[98:99], v[2:3] op_sel_hi:[1,0]
	s_waitcnt vmcnt(0)
	v_pk_mul_f32 v[46:47], v[46:47], v[74:75]
	v_pk_mul_f32 v[44:45], v[44:45], v[76:77]
	v_pk_mul_f32 v[46:47], v[50:51], v[46:47]
	v_pk_mul_f32 v[44:45], v[48:49], v[44:45]
	v_lshlrev_b32_e32 v48, 16, v72
	v_cvt_pk_bf16_f32 v44, v44, v45
	v_cvt_pk_bf16_f32 v45, v46, v47
	global_store_dwordx2 v[42:43], v[44:45], off offset:96
	global_load_dwordx4 v[44:47], v[40:41], off offset:256
	v_and_b32_e32 v49, 0xffff0000, v72
	v_lshlrev_b32_e32 v72, 16, v73
	v_and_b32_e32 v73, 0xffff0000, v73
	v_mul_f32_e32 v50, 0xbfb8aa3b, v48
	v_mul_f32_e32 v51, 0xbfb8aa3b, v49
	v_mul_f32_e32 v74, 0xbfb8aa3b, v72
	v_mul_f32_e32 v75, 0xbfb8aa3b, v73
	v_exp_f32_e32 v50, v50
	v_exp_f32_e32 v51, v51
	v_exp_f32_e32 v74, v74
	v_exp_f32_e32 v75, v75
	v_add_f32_e32 v50, 1.0, v50
	v_add_f32_e32 v51, 1.0, v51
	v_add_f32_e32 v74, 1.0, v74
	v_add_f32_e32 v75, 1.0, v75
	v_rcp_f32_e32 v50, v50
	v_rcp_f32_e32 v51, v51
	v_rcp_f32_e32 v74, v74
	v_rcp_f32_e32 v75, v75
	v_pk_mul_f32 v[48:49], v[50:51], v[48:49]
	v_pk_mul_f32 v[50:51], v[74:75], v[72:73]
	v_pk_mul_f32 v[72:73], v[104:105], v[2:3] op_sel_hi:[1,0]
	v_pk_mul_f32 v[74:75], v[106:107], v[2:3] op_sel_hi:[1,0]
	s_waitcnt vmcnt(0)
	v_pk_mul_f32 v[46:47], v[46:47], v[72:73]
	v_pk_mul_f32 v[44:45], v[44:45], v[74:75]
	v_pk_mul_f32 v[46:47], v[50:51], v[46:47]
	v_pk_mul_f32 v[44:45], v[48:49], v[44:45]
	v_lshlrev_b32_e32 v48, 16, v70
	v_cvt_pk_bf16_f32 v44, v44, v45
	v_cvt_pk_bf16_f32 v45, v46, v47
	global_store_dwordx2 v[42:43], v[44:45], off offset:128
	global_load_dwordx4 v[44:47], v[40:41], off offset:320
	v_and_b32_e32 v49, 0xffff0000, v70
	v_lshlrev_b32_e32 v70, 16, v71
	v_and_b32_e32 v71, 0xffff0000, v71
	v_mul_f32_e32 v50, 0xbfb8aa3b, v48
	v_mul_f32_e32 v51, 0xbfb8aa3b, v49
	v_mul_f32_e32 v72, 0xbfb8aa3b, v70
	v_mul_f32_e32 v73, 0xbfb8aa3b, v71
	v_exp_f32_e32 v50, v50
	v_exp_f32_e32 v51, v51
	v_exp_f32_e32 v72, v72
	v_exp_f32_e32 v73, v73
	v_add_f32_e32 v50, 1.0, v50
	v_add_f32_e32 v51, 1.0, v51
	v_add_f32_e32 v72, 1.0, v72
	v_add_f32_e32 v73, 1.0, v73
	v_rcp_f32_e32 v50, v50
	v_rcp_f32_e32 v51, v51
	v_rcp_f32_e32 v72, v72
	v_rcp_f32_e32 v73, v73
	v_pk_mul_f32 v[48:49], v[50:51], v[48:49]
	v_pk_mul_f32 v[50:51], v[72:73], v[70:71]
	v_pk_mul_f32 v[70:71], v[108:109], v[2:3] op_sel_hi:[1,0]
	v_pk_mul_f32 v[72:73], v[110:111], v[2:3] op_sel_hi:[1,0]
	s_waitcnt vmcnt(0)
	v_pk_mul_f32 v[46:47], v[46:47], v[70:71]
	v_pk_mul_f32 v[44:45], v[44:45], v[72:73]
	v_pk_mul_f32 v[46:47], v[50:51], v[46:47]
	v_pk_mul_f32 v[44:45], v[48:49], v[44:45]
	v_lshlrev_b32_e32 v48, 16, v68
	v_cvt_pk_bf16_f32 v44, v44, v45
	v_cvt_pk_bf16_f32 v45, v46, v47
	global_store_dwordx2 v[42:43], v[44:45], off offset:160
	global_load_dwordx4 v[44:47], v[40:41], off offset:384
	v_and_b32_e32 v49, 0xffff0000, v68
	v_lshlrev_b32_e32 v68, 16, v69
	v_and_b32_e32 v69, 0xffff0000, v69
	v_mul_f32_e32 v50, 0xbfb8aa3b, v48
	v_mul_f32_e32 v51, 0xbfb8aa3b, v49
	v_mul_f32_e32 v70, 0xbfb8aa3b, v68
	v_mul_f32_e32 v71, 0xbfb8aa3b, v69
	v_exp_f32_e32 v50, v50
	v_exp_f32_e32 v51, v51
	v_exp_f32_e32 v70, v70
	v_exp_f32_e32 v71, v71
	v_add_f32_e32 v50, 1.0, v50
	v_add_f32_e32 v51, 1.0, v51
	v_add_f32_e32 v70, 1.0, v70
	v_add_f32_e32 v71, 1.0, v71
	v_rcp_f32_e32 v50, v50
	v_rcp_f32_e32 v51, v51
	v_rcp_f32_e32 v70, v70
	v_rcp_f32_e32 v71, v71
	v_pk_mul_f32 v[48:49], v[50:51], v[48:49]
	v_pk_mul_f32 v[50:51], v[70:71], v[68:69]
	v_pk_mul_f32 v[68:69], v[112:113], v[2:3] op_sel_hi:[1,0]
	v_pk_mul_f32 v[70:71], v[114:115], v[2:3] op_sel_hi:[1,0]
	s_waitcnt vmcnt(0)
	v_pk_mul_f32 v[46:47], v[68:69], v[46:47]
	v_pk_mul_f32 v[44:45], v[70:71], v[44:45]
	v_pk_mul_f32 v[46:47], v[50:51], v[46:47]
	v_pk_mul_f32 v[44:45], v[48:49], v[44:45]
	v_lshlrev_b32_e32 v50, 16, v67
	v_cvt_pk_bf16_f32 v44, v44, v45
	v_cvt_pk_bf16_f32 v45, v46, v47
	global_store_dwordx2 v[42:43], v[44:45], off offset:192
	global_load_dwordx4 v[44:47], v[40:41], off offset:448
	v_lshlrev_b32_e32 v40, 16, v66
	v_and_b32_e32 v41, 0xffff0000, v66
	v_and_b32_e32 v51, 0xffff0000, v67
	v_mul_f32_e32 v48, 0xbfb8aa3b, v40
	v_mul_f32_e32 v49, 0xbfb8aa3b, v41
	v_mul_f32_e32 v66, 0xbfb8aa3b, v50
	v_mul_f32_e32 v67, 0xbfb8aa3b, v51
	v_exp_f32_e32 v48, v48
	v_exp_f32_e32 v49, v49
	v_exp_f32_e32 v66, v66
	v_exp_f32_e32 v67, v67
	v_add_f32_e32 v48, 1.0, v48
	v_add_f32_e32 v49, 1.0, v49
	v_add_f32_e32 v66, 1.0, v66
	v_add_f32_e32 v67, 1.0, v67
	v_rcp_f32_e32 v48, v48
	v_rcp_f32_e32 v49, v49
	v_rcp_f32_e32 v66, v66
	v_rcp_f32_e32 v67, v67
	v_pk_mul_f32 v[40:41], v[48:49], v[40:41]
	v_pk_mul_f32 v[48:49], v[66:67], v[50:51]
	s_waitcnt vmcnt(0)
	v_pk_mul_f32 v[38:39], v[38:39], v[44:45]
	v_pk_mul_f32 v[36:37], v[36:37], v[46:47]
	v_pk_mul_f32 v[38:39], v[40:41], v[38:39]
	v_pk_mul_f32 v[36:37], v[48:49], v[36:37]
	v_cvt_pk_bf16_f32 v38, v38, v39
	v_cvt_pk_bf16_f32 v39, v36, v37
	global_store_dwordx2 v[42:43], v[38:39], off offset:224
	s_waitcnt lgkmcnt(0)
	s_barrier
	s_cbranch_vccz .LBB0_768
.LBB0_764:
	s_mov_b32 s100, 0
	s_waitcnt vmcnt(0)
	ds_write_b128 v1, v[4:7]
	ds_write_b128 v1, v[8:11] offset:4352
	ds_write_b128 v1, v[12:15] offset:8704
	ds_write_b128 v1, v[16:19] offset:13056
	ds_write_b128 v1, v[20:23] offset:17408
	ds_write_b128 v1, v[24:27] offset:21760
	ds_write_b128 v1, v[28:31] offset:26112
	ds_write_b128 v1, v[32:35] offset:30464
	s_waitcnt lgkmcnt(0)
	s_barrier
	s_add_i32 s7, s10, s20
	s_cmpk_gt_i32 s7, 0x3ff
	s_cselect_b64 s[4:5], -1, 0
	s_cmpk_lt_i32 s7, 0x400
	s_mov_b64 s[2:3], -1
	s_cbranch_scc1 .LBB0_766
	v_readlane_b32 s2, v254, 42
	s_add_i32 s8, s9, s2
	s_mov_b64 s[2:3], 0
.LBB0_766:
	s_andn2_b64 vcc, exec, s[2:3]
	s_cbranch_vccnz .LBB0_763
	v_readlane_b32 s3, v254, 42
	s_add_i32 s8, s3, s9
	s_and_b32 s3, s8, 0xf0
	s_and_b32 s11, s7, 0x7fffff00
	s_bfe_u32 s2, s7, 0x40004
	s_or_b32 s3, s11, s3
	s_or_b32 s2, s3, s2
	s_lshl_b32 s2, s2, 1
	s_add_i32 s2, s2, s6
	s_ashr_i32 s3, s2, 31
	s_lshl_b64 s[2:3], s[2:3], 15
	v_lshl_add_u64 v[28:29], v[54:55], 0, s[2:3]
	v_add_co_u32_e32 v8, vcc, 0x1000, v28
	s_nop 1
	v_addc_co_u32_e32 v9, vcc, 0, v29, vcc
	v_add_co_u32_e32 v12, vcc, s12, v28
	s_nop 0
	v_addc_co_u32_e32 v13, vcc, 0, v29, vcc
	v_add_co_u32_e32 v16, vcc, 0x3000, v28
	s_nop 1
	v_addc_co_u32_e32 v17, vcc, 0, v29, vcc
	v_add_co_u32_e32 v20, vcc, 0x4000, v28
	s_nop 0
	v_addc_co_u32_e32 v21, vcc, 0, v29, vcc
	v_add_co_u32_e32 v24, vcc, 0x5000, v28
	s_nop 1
	v_addc_co_u32_e32 v25, vcc, 0, v29, vcc
	v_add_co_u32_e32 v30, vcc, 0x6000, v28
	s_nop 0
	v_addc_co_u32_e32 v31, vcc, 0, v29, vcc
	v_add_co_u32_e32 v32, vcc, 0x7000, v28
	s_nop 1
	v_addc_co_u32_e32 v33, vcc, 0, v29, vcc
	s_nop 0
	s_mov_b32 s100, 1
	s_branch .LBB0_763

	.amdhsa_kernel _Z8mega_fwd8MegaArgs
		.amdhsa_group_segment_fixed_size 0
		.amdhsa_private_segment_fixed_size 0
		.amdhsa_kernarg_size 432
		.amdhsa_user_sgpr_count 2
		.amdhsa_user_sgpr_dispatch_ptr 0
		.amdhsa_user_sgpr_queue_ptr 0
		.amdhsa_user_sgpr_kernarg_segment_ptr 1
		.amdhsa_user_sgpr_dispatch_id 0
		.amdhsa_user_sgpr_kernarg_preload_length 0
		.amdhsa_user_sgpr_kernarg_preload_offset 0
		.amdhsa_user_sgpr_private_segment_size 0
		.amdhsa_uses_dynamic_stack 0
		.amdhsa_enable_private_segment 0
		.amdhsa_system_sgpr_workgroup_id_x 1
		.amdhsa_system_sgpr_workgroup_id_y 0
		.amdhsa_system_sgpr_workgroup_id_z 0
		.amdhsa_system_sgpr_workgroup_info 0
		.amdhsa_system_vgpr_workitem_id 0
		.amdhsa_next_free_vgpr 255
		.amdhsa_next_free_sgpr 102
		.amdhsa_accum_offset 256
		.amdhsa_reserve_vcc 1
		.amdhsa_float_round_mode_32 0
		.amdhsa_float_round_mode_16_64 0
		.amdhsa_float_denorm_mode_32 3
		.amdhsa_float_denorm_mode_16_64 3
		.amdhsa_dx10_clamp 1
		.amdhsa_ieee_mode 1
		.amdhsa_fp16_overflow 0
		.amdhsa_tg_split 0
		.amdhsa_exception_fp_ieee_invalid_op 0
		.amdhsa_exception_fp_denorm_src 0
		.amdhsa_exception_fp_ieee_div_zero 0
		.amdhsa_exception_fp_ieee_overflow 0
		.amdhsa_exception_fp_ieee_underflow 0
		.amdhsa_exception_fp_ieee_inexact 0
		.amdhsa_exception_int_div_zero 0
	.end_amdhsa_kernel

amdhsa.kernels:
  - .agpr_count:     0
    .args:
      - .offset:         0
        .size:           176
        .value_kind:     by_value
      - .offset:         176
        .size:           4
        .value_kind:     hidden_block_count_x
      - .offset:         180
        .size:           4
        .value_kind:     hidden_block_count_y
      - .offset:         184
        .size:           4
        .value_kind:     hidden_block_count_z
      - .offset:         188
        .size:           2
        .value_kind:     hidden_group_size_x
      - .offset:         190
        .size:           2
        .value_kind:     hidden_group_size_y
      - .offset:         192
        .size:           2
        .value_kind:     hidden_group_size_z
      - .offset:         194
        .size:           2
        .value_kind:     hidden_remainder_x
      - .offset:         196
        .size:           2
        .value_kind:     hidden_remainder_y
      - .offset:         198
        .size:           2
        .value_kind:     hidden_remainder_z
      - .offset:         216
        .size:           8
        .value_kind:     hidden_global_offset_x
      - .offset:         224
        .size:           8
        .value_kind:     hidden_global_offset_y
      - .offset:         232
        .size:           8
        .value_kind:     hidden_global_offset_z
      - .offset:         240
        .size:           2
        .value_kind:     hidden_grid_dims
      - .offset:         296
        .size:           4
        .value_kind:     hidden_dynamic_lds_size
    .group_segment_fixed_size: 0
    .kernarg_segment_align: 8
    .kernarg_segment_size: 432
    .language:       OpenCL C
    .language_version:
      - 2
      - 0
    .max_flat_workgroup_size: 512
    .name:           _Z8mega_fwd8MegaArgs
    .private_segment_fixed_size: 0
    .sgpr_count:     108
    .sgpr_spill_count: 289
    .symbol:         _Z8mega_fwd8MegaArgs.kd
    .uniform_work_group_size: 1
    .uses_dynamic_stack: false
    .vgpr_count:     255
    .vgpr_spill_count: 0
    .wavefront_size: 64
